# session best plus sc1 (L1 bypass) on the two streamed idx/bary input loads
# baseline (speedup 1.0000x reference)
.Lwarm_skip:
	s_or_b64 exec, exec, s[10:11]
	v_mad_u64_u32 v[2:3], s[6:7], v71, 12, s[6:7]
	v_lshlrev_b32_e32 v4, 2, v71
	v_mov_b32_e32 v5, v69
	s_movk_i32 s6, 0xfe00
	v_lshl_add_u64 v[4:5], s[8:9], 0, v[4:5]
	v_lshl_add_u64 v[8:9], v[2:3], 0, v[6:7]
	s_mov_b32 s7, -1
	v_lshl_add_u64 v[4:5], v[4:5], 0, v[6:7]
	v_lshl_add_u64 v[2:3], v[8:9], 0, s[6:7]
	v_cmp_gt_u32_e32 vcc, 32, v1
	v_lshlrev_b32_e32 v33, 12, v10
	v_add_u32_e32 v34, v33, v6
	v_cndmask_b32_e32 v3, v3, v5, vcc
	v_cndmask_b32_e32 v2, v2, v4, vcc
	global_load_dwordx4 v[2:5], v[2:3], off sc1
	v_and_b32_e32 v72, 1, v0
	v_lshl_add_u32 v0, v32, 4, v33
	v_lshlrev_b32_e32 v73, 4, v32
	v_lshlrev_b32_e32 v74, 6, v72
	v_xor_b32_e32 v73, v73, v74
	v_lshl_add_u32 v73, v72, 11, v73
	v_lshl_add_u32 v73, v10, 12, v73
	v_and_b32_e32 v74, 31, v1
	v_lshrrev_b32_e32 v75, 5, v1
	v_lshl_or_b32 v76, v74, 2, v71
	v_lshlrev_b32_e32 v74, 4, v74
	v_lshlrev_b32_e32 v77, 6, v75
	v_xor_b32_e32 v74, v74, v77
	v_lshl_add_u32 v74, v75, 11, v74
	v_lshl_add_u32 v74, v10, 12, v74
	v_lshlrev_b32_e32 v77, 7, v71
	v_and_b32_e32 v77, 0xe000000, v77
	v_and_b32_e32 v76, 0x3fffc, v76
	v_lshlrev_b32_e32 v75, 21, v75
	v_or3_b32 v75, v77, v75, v76
	v_lshlrev_b32_e32 v75, 2, v75
	s_mul_i32 s6, s4, 0x138800
	s_mul_hi_i32 s5, s4, 0x138800
	s_add_u32 s2, s2, s6
	s_addc_u32 s3, s3, s5
	global_load_dwordx4 v[28:31], v[8:9], off offset:512 sc1
	s_waitcnt vmcnt(1)
	ds_write_b128 v34, v[2:5]
	ds_read_b128 v[4:7], v0
	v_lshlrev_b32_e32 v0, 4, v72
	s_waitcnt lgkmcnt(0)
	v_max_i32_e32 v1, 0, v4
	v_max_i32_e32 v2, 0, v5
	v_max_i32_e32 v3, 0, v6
	v_max_i32_e32 v8, 0, v7
	v_lshl_or_b32 v35, v1, 7, v0
	v_lshl_or_b32 v36, v2, 7, v0
	v_lshl_or_b32 v37, v3, 7, v0
	v_lshl_or_b32 v38, v8, 7, v0
	global_load_dwordx4 v[20:23], v35, s[2:3]
	global_load_dwordx4 v[16:19], v35, s[2:3] offset:32
	global_load_dwordx4 v[8:11], v35, s[2:3] offset:64
	global_load_dwordx4 v[64:67], v36, s[2:3]
	global_load_dwordx4 v[60:63], v36, s[2:3] offset:32
	global_load_dwordx4 v[56:59], v36, s[2:3] offset:64
	global_load_dwordx4 v[52:55], v37, s[2:3]
	global_load_dwordx4 v[48:51], v37, s[2:3] offset:32
	global_load_dwordx4 v[44:47], v37, s[2:3] offset:64
	global_load_dwordx4 v[24:27], v38, s[2:3]
	global_load_dwordx4 v[12:15], v38, s[2:3] offset:32
	global_load_dwordx4 v[0:3], v38, s[2:3] offset:64
	s_waitcnt vmcnt(12)
	ds_write_b128 v34, v[28:31] offset:1024
	v_mul_u32_u24_e32 v28, 48, v32
	v_cmp_lt_i32_e32 vcc, -1, v4
	v_add_u32_e32 v31, v33, v28
	v_mov_b32_e32 v28, 0
	s_and_saveexec_b64 s[2:3], vcc
	ds_read_b32 v28, v31 offset:512
	s_or_b64 exec, exec, s[2:3]
	s_and_saveexec_b64 s[2:3], vcc
	ds_read_b32 v69, v31 offset:516
	s_or_b64 exec, exec, s[2:3]
	v_mov_b32_e32 v29, 0
	v_mov_b32_e32 v4, 0
	s_and_saveexec_b64 s[2:3], vcc
	ds_read_b32 v4, v31 offset:520
	s_or_b64 exec, exec, s[2:3]
	s_waitcnt vmcnt(11) lgkmcnt(0)
	v_fma_mix_f32 v30, v28, v20, v29 op_sel_hi:[0,1,0]
	v_fma_mix_f32 v20, v28, v20, v29 op_sel:[0,1,0] op_sel_hi:[0,1,0]
	v_fma_mix_f32 v32, v28, v21, v29 op_sel_hi:[0,1,0]
	v_fma_mix_f32 v21, v28, v21, v29 op_sel:[0,1,0] op_sel_hi:[0,1,0]
	v_fma_mix_f32 v33, v28, v22, v29 op_sel_hi:[0,1,0]
	v_fma_mix_f32 v22, v28, v22, v29 op_sel:[0,1,0] op_sel_hi:[0,1,0]
	v_fma_mix_f32 v34, v28, v23, v29 op_sel_hi:[0,1,0]
	v_fma_mix_f32 v23, v28, v23, v29 op_sel:[0,1,0] op_sel_hi:[0,1,0]
	s_waitcnt vmcnt(10)
	v_fma_mix_f32 v28, v69, v16, v30 op_sel_hi:[0,1,0]
	v_fma_mix_f32 v16, v69, v16, v20 op_sel:[0,1,0] op_sel_hi:[0,1,0]
	v_fma_mix_f32 v20, v69, v17, v32 op_sel_hi:[0,1,0]
	v_cmp_lt_i32_e32 vcc, -1, v5
	v_fma_mix_f32 v17, v69, v17, v21 op_sel:[0,1,0] op_sel_hi:[0,1,0]
	v_fma_mix_f32 v21, v69, v18, v33 op_sel_hi:[0,1,0]
	v_fma_mix_f32 v18, v69, v18, v22 op_sel:[0,1,0] op_sel_hi:[0,1,0]
	v_fma_mix_f32 v22, v69, v19, v34 op_sel_hi:[0,1,0]
	v_fma_mix_f32 v19, v69, v19, v23 op_sel:[0,1,0] op_sel_hi:[0,1,0]
	s_waitcnt vmcnt(9)
	v_fma_mix_f32 v40, v4, v8, v28 op_sel_hi:[0,1,0]
	v_fma_mix_f32 v36, v4, v8, v16 op_sel:[0,1,0] op_sel_hi:[0,1,0]
	v_fma_mix_f32 v32, v4, v9, v20 op_sel_hi:[0,1,0]
	v_fma_mix_f32 v28, v4, v9, v17 op_sel:[0,1,0] op_sel_hi:[0,1,0]
	v_fma_mix_f32 v20, v4, v10, v21 op_sel_hi:[0,1,0]
	v_fma_mix_f32 v16, v4, v10, v18 op_sel:[0,1,0] op_sel_hi:[0,1,0]
	v_fma_mix_f32 v8, v4, v11, v22 op_sel_hi:[0,1,0]
	v_fma_mix_f32 v4, v4, v11, v19 op_sel:[0,1,0] op_sel_hi:[0,1,0]
	s_and_saveexec_b64 s[2:3], vcc
	ds_read_b32 v29, v31 offset:524
	s_or_b64 exec, exec, s[2:3]
	v_mov_b32_e32 v5, 0
	v_mov_b32_e32 v9, 0
	s_and_saveexec_b64 s[2:3], vcc
	ds_read_b32 v9, v31 offset:528
	s_or_b64 exec, exec, s[2:3]
	s_and_saveexec_b64 s[2:3], vcc
	ds_read_b32 v5, v31 offset:532
	s_or_b64 exec, exec, s[2:3]
	v_mov_b32_e32 v10, 0
	s_waitcnt vmcnt(8) lgkmcnt(0)
	v_fma_mix_f32 v18, v29, v65, v10 op_sel_hi:[0,1,0]
	v_fma_mix_f32 v17, v29, v64, v10 op_sel:[0,1,0] op_sel_hi:[0,1,0]
	v_fma_mix_f32 v21, v29, v66, v10 op_sel_hi:[0,1,0]
	v_fma_mix_f32 v11, v29, v64, v10 op_sel_hi:[0,1,0]
	v_fma_mix_f32 v19, v29, v65, v10 op_sel:[0,1,0] op_sel_hi:[0,1,0]
	s_waitcnt vmcnt(7)
	v_fma_mix_f32 v18, v9, v61, v18 op_sel_hi:[0,1,0]
	v_fma_mix_f32 v22, v29, v66, v10 op_sel:[0,1,0] op_sel_hi:[0,1,0]
	v_fma_mix_f32 v23, v29, v67, v10 op_sel_hi:[0,1,0]
	v_fma_mix_f32 v29, v29, v67, v10 op_sel:[0,1,0] op_sel_hi:[0,1,0]
	v_fma_mix_f32 v17, v9, v60, v17 op_sel:[0,1,0] op_sel_hi:[0,1,0]
	v_fma_mix_f32 v21, v9, v62, v21 op_sel_hi:[0,1,0]
	s_waitcnt vmcnt(6)
	v_fma_mix_f32 v33, v5, v57, v18 op_sel_hi:[0,1,0]
	v_cmp_lt_i32_e32 vcc, -1, v6
	v_mov_b32_e32 v18, 0
	v_fma_mix_f32 v11, v9, v60, v11 op_sel_hi:[0,1,0]
	v_fma_mix_f32 v19, v9, v61, v19 op_sel:[0,1,0] op_sel_hi:[0,1,0]
	v_fma_mix_f32 v22, v9, v62, v22 op_sel:[0,1,0] op_sel_hi:[0,1,0]
	v_fma_mix_f32 v23, v9, v63, v23 op_sel_hi:[0,1,0]
	v_fma_mix_f32 v30, v9, v63, v29 op_sel:[0,1,0] op_sel_hi:[0,1,0]
	v_fma_mix_f32 v37, v5, v56, v17 op_sel:[0,1,0] op_sel_hi:[0,1,0]
	s_nop 0
	v_fma_mix_f32 v41, v5, v56, v11 op_sel_hi:[0,1,0]
	v_fma_mix_f32 v29, v5, v57, v19 op_sel:[0,1,0] op_sel_hi:[0,1,0]
	v_fma_mix_f32 v21, v5, v58, v21 op_sel_hi:[0,1,0]
	v_fma_mix_f32 v17, v5, v58, v22 op_sel:[0,1,0] op_sel_hi:[0,1,0]
	v_fma_mix_f32 v9, v5, v59, v23 op_sel_hi:[0,1,0]
	v_fma_mix_f32 v5, v5, v59, v30 op_sel:[0,1,0] op_sel_hi:[0,1,0]
	s_and_saveexec_b64 s[2:3], vcc
	ds_read_b32 v18, v31 offset:536
	s_or_b64 exec, exec, s[2:3]
	s_and_saveexec_b64 s[2:3], vcc
	ds_read_b32 v10, v31 offset:540
	s_or_b64 exec, exec, s[2:3]
	v_mov_b32_e32 v11, 0
	v_mov_b32_e32 v6, 0
	s_and_saveexec_b64 s[2:3], vcc
	ds_read_b32 v6, v31 offset:544
	s_or_b64 exec, exec, s[2:3]
	s_waitcnt vmcnt(5) lgkmcnt(0)
	v_fma_mix_f32 v22, v18, v52, v11 op_sel:[0,1,0] op_sel_hi:[0,1,0]
	v_fma_mix_f32 v30, v18, v53, v11 op_sel:[0,1,0] op_sel_hi:[0,1,0]
	v_fma_mix_f32 v19, v18, v52, v11 op_sel_hi:[0,1,0]
	v_fma_mix_f32 v23, v18, v53, v11 op_sel_hi:[0,1,0]
	v_fma_mix_f32 v34, v18, v54, v11 op_sel_hi:[0,1,0]
	v_fma_mix_f32 v35, v18, v54, v11 op_sel:[0,1,0] op_sel_hi:[0,1,0]
	v_fma_mix_f32 v38, v18, v55, v11 op_sel_hi:[0,1,0]
	v_fma_mix_f32 v18, v18, v55, v11 op_sel:[0,1,0] op_sel_hi:[0,1,0]
	s_waitcnt vmcnt(4)
	v_fma_mix_f32 v22, v10, v48, v22 op_sel:[0,1,0] op_sel_hi:[0,1,0]
	v_fma_mix_f32 v30, v10, v49, v30 op_sel:[0,1,0] op_sel_hi:[0,1,0]
	v_cmp_lt_i32_e32 vcc, -1, v7
	v_fma_mix_f32 v19, v10, v48, v19 op_sel_hi:[0,1,0]
	v_fma_mix_f32 v23, v10, v49, v23 op_sel_hi:[0,1,0]
	v_fma_mix_f32 v39, v10, v50, v34 op_sel_hi:[0,1,0]
	v_fma_mix_f32 v35, v10, v50, v35 op_sel:[0,1,0] op_sel_hi:[0,1,0]
	v_fma_mix_f32 v43, v10, v51, v38 op_sel_hi:[0,1,0]
	v_fma_mix_f32 v48, v10, v51, v18 op_sel:[0,1,0] op_sel_hi:[0,1,0]
	s_waitcnt vmcnt(3)
	v_fma_mix_f32 v42, v6, v44, v19 op_sel_hi:[0,1,0]
	v_fma_mix_f32 v38, v6, v44, v22 op_sel:[0,1,0] op_sel_hi:[0,1,0]
	v_fma_mix_f32 v34, v6, v45, v23 op_sel_hi:[0,1,0]
	v_fma_mix_f32 v30, v6, v45, v30 op_sel:[0,1,0] op_sel_hi:[0,1,0]
	v_fma_mix_f32 v22, v6, v46, v39 op_sel_hi:[0,1,0]
	v_fma_mix_f32 v18, v6, v46, v35 op_sel:[0,1,0] op_sel_hi:[0,1,0]
	v_fma_mix_f32 v10, v6, v47, v43 op_sel_hi:[0,1,0]
	v_fma_mix_f32 v6, v6, v47, v48 op_sel:[0,1,0] op_sel_hi:[0,1,0]
	s_and_saveexec_b64 s[2:3], vcc
	ds_read_b32 v11, v31 offset:548
	s_or_b64 exec, exec, s[2:3]
	s_load_dwordx2 s[0:1], s[0:1], 0x18
	s_ashr_i32 s5, s4, 31
	v_mov_b32_e32 v7, 0
	v_mov_b32_e32 v19, 0
	s_and_saveexec_b64 s[2:3], vcc
	ds_read_b32 v19, v31 offset:552
	s_or_b64 exec, exec, s[2:3]
	s_and_saveexec_b64 s[2:3], vcc
	ds_read_b32 v7, v31 offset:556
	s_or_b64 exec, exec, s[2:3]
	v_mov_b32_e32 v23, 0
	s_waitcnt vmcnt(2) lgkmcnt(0)
	v_fma_mix_f32 v31, v11, v24, v23 op_sel_hi:[0,1,0]
	v_fma_mix_f32 v24, v11, v24, v23 op_sel:[0,1,0] op_sel_hi:[0,1,0]
	v_fma_mix_f32 v35, v11, v25, v23 op_sel_hi:[0,1,0]
	v_fma_mix_f32 v25, v11, v25, v23 op_sel:[0,1,0] op_sel_hi:[0,1,0]
	v_fma_mix_f32 v39, v11, v26, v23 op_sel_hi:[0,1,0]
	v_fma_mix_f32 v26, v11, v26, v23 op_sel:[0,1,0] op_sel_hi:[0,1,0]
	v_fma_mix_f32 v43, v11, v27, v23 op_sel_hi:[0,1,0]
	v_fma_mix_f32 v11, v11, v27, v23 op_sel:[0,1,0] op_sel_hi:[0,1,0]
	s_waitcnt vmcnt(1)
	v_fma_mix_f32 v23, v19, v12, v31 op_sel_hi:[0,1,0]
	s_lshl_b64 s[2:3], s[4:5], 24
	v_fma_mix_f32 v12, v19, v12, v24 op_sel:[0,1,0] op_sel_hi:[0,1,0]
	v_fma_mix_f32 v24, v19, v13, v35 op_sel_hi:[0,1,0]
	v_fma_mix_f32 v13, v19, v13, v25 op_sel:[0,1,0] op_sel_hi:[0,1,0]
	v_fma_mix_f32 v25, v19, v14, v39 op_sel_hi:[0,1,0]
	v_fma_mix_f32 v14, v19, v14, v26 op_sel:[0,1,0] op_sel_hi:[0,1,0]
	v_fma_mix_f32 v26, v19, v15, v43 op_sel_hi:[0,1,0]
	v_fma_mix_f32 v15, v19, v15, v11 op_sel:[0,1,0] op_sel_hi:[0,1,0]
	s_add_u32 s0, s0, s2
	s_addc_u32 s1, s1, s3
	s_add_u32 s2, s0, 0x100000
	s_addc_u32 s3, s1, 0
	s_add_u32 s4, s0, 0x200000
	s_addc_u32 s5, s1, 0
	s_add_u32 s6, s0, 0x300000
	s_addc_u32 s7, s1, 0
	s_add_u32 s8, s0, 0x400000
	s_addc_u32 s9, s1, 0
	s_add_u32 s10, s0, 0x500000
	s_addc_u32 s11, s1, 0
	s_add_u32 s12, s0, 0x600000
	s_addc_u32 s13, s1, 0
	s_add_u32 s14, s0, 0x700000
	s_addc_u32 s15, s1, 0
	s_waitcnt vmcnt(0)
	v_fma_mix_f32 v43, v7, v0, v23 op_sel_hi:[0,1,0]
	v_fma_mix_f32 v23, v7, v2, v25 op_sel_hi:[0,1,0]
	v_fma_mix_f32 v19, v7, v2, v14 op_sel:[0,1,0] op_sel_hi:[0,1,0]
	v_fma_mix_f32 v39, v7, v0, v12 op_sel:[0,1,0] op_sel_hi:[0,1,0]
	v_fma_mix_f32 v35, v7, v1, v24 op_sel_hi:[0,1,0]
	v_fma_mix_f32 v31, v7, v1, v13 op_sel:[0,1,0] op_sel_hi:[0,1,0]
	v_fma_mix_f32 v11, v7, v3, v26 op_sel_hi:[0,1,0]
	v_fma_mix_f32 v7, v7, v3, v15 op_sel:[0,1,0] op_sel_hi:[0,1,0]
	ds_write_b128 v73, v[40:43]
	ds_write_b128 v73, v[36:39] offset:512
	ds_write_b128 v73, v[32:35] offset:1024
	ds_write_b128 v73, v[28:31] offset:1536
	ds_read_b128 v[44:47], v74
	ds_read_b128 v[48:51], v74 offset:512
	ds_read_b128 v[52:55], v74 offset:1024
	ds_read_b128 v[56:59], v74 offset:1536
	ds_write_b128 v73, v[20:23]
	ds_write_b128 v73, v[16:19] offset:512
	ds_write_b128 v73, v[8:11] offset:1024
	ds_write_b128 v73, v[4:7] offset:1536
	s_waitcnt lgkmcnt(7)
	global_store_dwordx4 v75, v[44:47], s[0:1] nt
	s_waitcnt lgkmcnt(6)
	global_store_dwordx4 v75, v[48:51], s[2:3] nt
	s_waitcnt lgkmcnt(5)
	global_store_dwordx4 v75, v[52:55], s[4:5] nt
	s_waitcnt lgkmcnt(4)
	global_store_dwordx4 v75, v[56:59], s[6:7] nt
	ds_read_b128 v[60:63], v74
	ds_read_b128 v[64:67], v74 offset:512
	ds_read_b128 v[0:3], v74 offset:1024
	ds_read_b128 v[12:15], v74 offset:1536
	s_waitcnt lgkmcnt(3)
	global_store_dwordx4 v75, v[60:63], s[8:9] nt
	s_waitcnt lgkmcnt(2)
	global_store_dwordx4 v75, v[64:67], s[10:11] nt
	s_waitcnt lgkmcnt(1)
	global_store_dwordx4 v75, v[0:3], s[12:13] nt
	s_waitcnt lgkmcnt(0)
	global_store_dwordx4 v75, v[12:15], s[14:15] nt
	s_endpgm
